# final RMSNorm phase rewritten by hand: 4-token batches, two register sets, next batch loads in flight (software pipelined), norm_final hoisted, ss partials by one lane-varying load + DPP tree
# speedup vs baseline: 1.0100x; 1.0100x over previous
.LBB0_3638:
	s_or_b64 exec, exec, s[6:7]
	s_lshr_b32 s1, s97, 3
	s_mul_i32 s1, s1, s64
	v_readlane_b32 s3, v254, 12
	s_and_b32 s0, s97, 7
	s_add_i32 s1, s1, s3
	s_cmp_eq_u32 s0, 0
	s_cselect_b32 s0, s1, s2
	s_waitcnt lgkmcnt(0)
	s_barrier
	s_lshl_b32 s1, s0, 3
	s_nop 0
	v_readfirstlane_b32 s0, v0
	s_lshl_b32 s13, s97, 3
	s_ashr_i32 s2, s0, 6
	s_add_i32 s12, s2, s1
	s_cmp_lt_i32 s12, 0x10000
	s_cbranch_scc0 .LBB0_3641
	s_load_dwordx4 s[4:7], s[90:91], 0xc0
	s_load_dwordx2 s[8:9], s[90:91], 0x28
	v_and_b32_e32 v1, 63, v0
	v_lshlrev_b32_e32 v2, 5, v1
	v_lshlrev_b32_e32 v3, 4, v1
	v_and_b32_e32 v4, 15, v1
	v_lshlrev_b32_e32 v4, 18, v4
	v_mov_b32_e32 v5, 0x358637bd
	s_lshl_b32 s20, s13, 2
	s_lshl_b32 s21, s13, 11
	s_lshl_b32 s22, s13, 12
	s_mul_i32 s23, s13, 7
	s_waitcnt lgkmcnt(0)
	global_load_dwordx4 v[8:11], v2, s[8:9]
	global_load_dwordx4 v[12:15], v2, s[8:9] offset:16
	global_load_dwordx4 v[16:19], v2, s[8:9] offset:2048
	global_load_dwordx4 v[20:23], v2, s[8:9] offset:2064
	s_ashr_i32 s15, s12, 31
	s_mov_b32 s14, s12
	s_lshl_b64 s[16:17], s[14:15], 2
	s_add_u32 s16, s16, 0x72000000
	s_addc_u32 s17, s17, 0
	s_add_u32 s16, s16, s6
	s_addc_u32 s17, s17, s7
	s_lshl_b64 s[18:19], s[14:15], 11
	s_add_u32 s18, s18, 0x26c00000
	s_addc_u32 s19, s19, 0
	s_add_u32 s18, s18, s6
	s_addc_u32 s19, s19, s7
	s_lshl_b64 s[24:25], s[14:15], 12
	s_add_u32 s24, s24, s4
	s_addc_u32 s25, s25, s5
	s_add_i32 s14, s12, s23
	s_cmp_lt_i32 s14, 0x10000
	s_cbranch_scc0 .Lfin_tail
	s_mov_b64 s[26:27], s[16:17]
	s_mov_b64 s[28:29], s[18:19]
	global_load_dword v40, v4, s[26:27]
	global_load_dwordx4 v[32:35], v3, s[28:29]
	global_load_dwordx4 v[36:39], v3, s[28:29] offset:1024
	s_add_u32 s16, s16, s20
	s_addc_u32 s17, s17, 0
	s_add_u32 s18, s18, s21
	s_addc_u32 s19, s19, 0
	s_add_i32 s12, s12, s13
	s_mov_b64 s[30:31], s[16:17]
	s_mov_b64 s[32:33], s[18:19]
	global_load_dword v50, v4, s[30:31]
	global_load_dwordx4 v[42:45], v3, s[32:33]
	global_load_dwordx4 v[46:49], v3, s[32:33] offset:1024
	s_add_u32 s16, s16, s20
	s_addc_u32 s17, s17, 0
	s_add_u32 s18, s18, s21
	s_addc_u32 s19, s19, 0
	s_add_i32 s12, s12, s13
	s_mov_b64 s[26:27], s[16:17]
	s_mov_b64 s[28:29], s[18:19]
	global_load_dword v60, v4, s[26:27]
	global_load_dwordx4 v[52:55], v3, s[28:29]
	global_load_dwordx4 v[56:59], v3, s[28:29] offset:1024
	s_add_u32 s16, s16, s20
	s_addc_u32 s17, s17, 0
	s_add_u32 s18, s18, s21
	s_addc_u32 s19, s19, 0
	s_add_i32 s12, s12, s13
	s_mov_b64 s[30:31], s[16:17]
	s_mov_b64 s[32:33], s[18:19]
	global_load_dword v70, v4, s[30:31]
	global_load_dwordx4 v[62:65], v3, s[32:33]
	global_load_dwordx4 v[66:69], v3, s[32:33] offset:1024
	s_add_u32 s16, s16, s20
	s_addc_u32 s17, s17, 0
	s_add_u32 s18, s18, s21
	s_addc_u32 s19, s19, 0
	s_add_i32 s12, s12, s13
	s_mov_b64 s[26:27], s[16:17]
	s_mov_b64 s[28:29], s[18:19]
	global_load_dword v80, v4, s[26:27]
	global_load_dwordx4 v[72:75], v3, s[28:29]
	global_load_dwordx4 v[76:79], v3, s[28:29] offset:1024
	s_add_u32 s16, s16, s20
	s_addc_u32 s17, s17, 0
	s_add_u32 s18, s18, s21
	s_addc_u32 s19, s19, 0
	s_add_i32 s12, s12, s13
	s_mov_b64 s[30:31], s[16:17]
	s_mov_b64 s[32:33], s[18:19]
	global_load_dword v90, v4, s[30:31]
	global_load_dwordx4 v[82:85], v3, s[32:33]
	global_load_dwordx4 v[86:89], v3, s[32:33] offset:1024
	s_add_u32 s16, s16, s20
	s_addc_u32 s17, s17, 0
	s_add_u32 s18, s18, s21
	s_addc_u32 s19, s19, 0
	s_add_i32 s12, s12, s13
	s_mov_b64 s[26:27], s[16:17]
	s_mov_b64 s[28:29], s[18:19]
	global_load_dword v100, v4, s[26:27]
	global_load_dwordx4 v[92:95], v3, s[28:29]
	global_load_dwordx4 v[96:99], v3, s[28:29] offset:1024
	s_add_u32 s16, s16, s20
	s_addc_u32 s17, s17, 0
	s_add_u32 s18, s18, s21
	s_addc_u32 s19, s19, 0
	s_add_i32 s12, s12, s13
	s_mov_b64 s[30:31], s[16:17]
	s_mov_b64 s[32:33], s[18:19]
	global_load_dword v110, v4, s[30:31]
	global_load_dwordx4 v[102:105], v3, s[32:33]
	global_load_dwordx4 v[106:109], v3, s[32:33] offset:1024
	s_add_u32 s16, s16, s20
	s_addc_u32 s17, s17, 0
	s_add_u32 s18, s18, s21
	s_addc_u32 s19, s19, 0
	s_add_i32 s12, s12, s13
	s_waitcnt vmcnt(21)
	v_add_f32_dpp v112, v40, v40 quad_perm:[1,0,3,2] row_mask:0xf bank_mask:0xf
	s_mov_b64 s[34:35], s[24:25]
	s_add_u32 s24, s24, s22
	v_add_f32_dpp v112, v112, v112 quad_perm:[2,3,0,1] row_mask:0xf bank_mask:0xf
	s_addc_u32 s25, s25, 0
	s_nop 0
	v_add_f32_dpp v112, v112, v112 row_half_mirror row_mask:0xf bank_mask:0xf
	s_nop 1
	v_add_f32_dpp v112, v112, v112 row_mirror row_mask:0xf bank_mask:0xf
	v_fmamk_f32 v112, v112, 0x3a800000, v5
	v_rsq_f32_e32 v114, v112
	v_lshlrev_b32_e32 v116, 16, v32
	v_and_b32_e32 v117, 0xffff0000, v32
	v_lshlrev_b32_e32 v118, 16, v33
	v_and_b32_e32 v119, 0xffff0000, v33
	v_lshlrev_b32_e32 v120, 16, v34
	v_and_b32_e32 v121, 0xffff0000, v34
	v_lshlrev_b32_e32 v122, 16, v35
	v_and_b32_e32 v123, 0xffff0000, v35
	v_lshlrev_b32_e32 v124, 16, v36
	v_and_b32_e32 v125, 0xffff0000, v36
	v_lshlrev_b32_e32 v126, 16, v37
	v_and_b32_e32 v127, 0xffff0000, v37
	v_lshlrev_b32_e32 v128, 16, v38
	v_and_b32_e32 v129, 0xffff0000, v38
	v_lshlrev_b32_e32 v130, 16, v39
	v_and_b32_e32 v131, 0xffff0000, v39
	v_pk_mul_f32 v[116:117], v[114:115], v[116:117] op_sel_hi:[0,1]
	v_pk_mul_f32 v[118:119], v[114:115], v[118:119] op_sel_hi:[0,1]
	v_pk_mul_f32 v[120:121], v[114:115], v[120:121] op_sel_hi:[0,1]
	v_pk_mul_f32 v[122:123], v[114:115], v[122:123] op_sel_hi:[0,1]
	v_pk_mul_f32 v[124:125], v[114:115], v[124:125] op_sel_hi:[0,1]
	v_pk_mul_f32 v[126:127], v[114:115], v[126:127] op_sel_hi:[0,1]
	v_pk_mul_f32 v[128:129], v[114:115], v[128:129] op_sel_hi:[0,1]
	v_pk_mul_f32 v[130:131], v[114:115], v[130:131] op_sel_hi:[0,1]
	v_pk_mul_f32 v[132:133], v[8:9], v[116:117]
	v_pk_mul_f32 v[134:135], v[10:11], v[118:119]
	v_pk_mul_f32 v[136:137], v[12:13], v[120:121]
	v_pk_mul_f32 v[138:139], v[14:15], v[122:123]
	v_pk_mul_f32 v[140:141], v[16:17], v[124:125]
	v_pk_mul_f32 v[142:143], v[18:19], v[126:127]
	v_pk_mul_f32 v[144:145], v[20:21], v[128:129]
	v_pk_mul_f32 v[146:147], v[22:23], v[130:131]
	global_store_dwordx4 v2, v[132:135], s[34:35]
	global_store_dwordx4 v2, v[136:139], s[34:35] offset:16
	global_store_dwordx4 v2, v[140:143], s[34:35] offset:2048
	global_store_dwordx4 v2, v[144:147], s[34:35] offset:2064
	s_waitcnt vmcnt(22)
	v_add_f32_dpp v112, v50, v50 quad_perm:[1,0,3,2] row_mask:0xf bank_mask:0xf
	s_mov_b64 s[36:37], s[24:25]
	s_add_u32 s24, s24, s22
	v_add_f32_dpp v112, v112, v112 quad_perm:[2,3,0,1] row_mask:0xf bank_mask:0xf
	s_addc_u32 s25, s25, 0
	s_nop 0
	v_add_f32_dpp v112, v112, v112 row_half_mirror row_mask:0xf bank_mask:0xf
	s_nop 1
	v_add_f32_dpp v112, v112, v112 row_mirror row_mask:0xf bank_mask:0xf
	v_fmamk_f32 v112, v112, 0x3a800000, v5
	v_rsq_f32_e32 v114, v112
	v_lshlrev_b32_e32 v116, 16, v42
	v_and_b32_e32 v117, 0xffff0000, v42
	v_lshlrev_b32_e32 v118, 16, v43
	v_and_b32_e32 v119, 0xffff0000, v43
	v_lshlrev_b32_e32 v120, 16, v44
	v_and_b32_e32 v121, 0xffff0000, v44
	v_lshlrev_b32_e32 v122, 16, v45
	v_and_b32_e32 v123, 0xffff0000, v45
	v_lshlrev_b32_e32 v124, 16, v46
	v_and_b32_e32 v125, 0xffff0000, v46
	v_lshlrev_b32_e32 v126, 16, v47
	v_and_b32_e32 v127, 0xffff0000, v47
	v_lshlrev_b32_e32 v128, 16, v48
	v_and_b32_e32 v129, 0xffff0000, v48
	v_lshlrev_b32_e32 v130, 16, v49
	v_and_b32_e32 v131, 0xffff0000, v49
	v_pk_mul_f32 v[116:117], v[114:115], v[116:117] op_sel_hi:[0,1]
	v_pk_mul_f32 v[118:119], v[114:115], v[118:119] op_sel_hi:[0,1]
	v_pk_mul_f32 v[120:121], v[114:115], v[120:121] op_sel_hi:[0,1]
	v_pk_mul_f32 v[122:123], v[114:115], v[122:123] op_sel_hi:[0,1]
	v_pk_mul_f32 v[124:125], v[114:115], v[124:125] op_sel_hi:[0,1]
	v_pk_mul_f32 v[126:127], v[114:115], v[126:127] op_sel_hi:[0,1]
	v_pk_mul_f32 v[128:129], v[114:115], v[128:129] op_sel_hi:[0,1]
	v_pk_mul_f32 v[130:131], v[114:115], v[130:131] op_sel_hi:[0,1]
	v_pk_mul_f32 v[132:133], v[8:9], v[116:117]
	v_pk_mul_f32 v[134:135], v[10:11], v[118:119]
	v_pk_mul_f32 v[136:137], v[12:13], v[120:121]
	v_pk_mul_f32 v[138:139], v[14:15], v[122:123]
	v_pk_mul_f32 v[140:141], v[16:17], v[124:125]
	v_pk_mul_f32 v[142:143], v[18:19], v[126:127]
	v_pk_mul_f32 v[144:145], v[20:21], v[128:129]
	v_pk_mul_f32 v[146:147], v[22:23], v[130:131]
	global_store_dwordx4 v2, v[132:135], s[36:37]
	global_store_dwordx4 v2, v[136:139], s[36:37] offset:16
	global_store_dwordx4 v2, v[140:143], s[36:37] offset:2048
	global_store_dwordx4 v2, v[144:147], s[36:37] offset:2064
	s_waitcnt vmcnt(23)
	v_add_f32_dpp v112, v60, v60 quad_perm:[1,0,3,2] row_mask:0xf bank_mask:0xf
	s_mov_b64 s[34:35], s[24:25]
	s_add_u32 s24, s24, s22
	v_add_f32_dpp v112, v112, v112 quad_perm:[2,3,0,1] row_mask:0xf bank_mask:0xf
	s_addc_u32 s25, s25, 0
	s_nop 0
	v_add_f32_dpp v112, v112, v112 row_half_mirror row_mask:0xf bank_mask:0xf
	s_nop 1
	v_add_f32_dpp v112, v112, v112 row_mirror row_mask:0xf bank_mask:0xf
	v_fmamk_f32 v112, v112, 0x3a800000, v5
	v_rsq_f32_e32 v114, v112
	v_lshlrev_b32_e32 v116, 16, v52
	v_and_b32_e32 v117, 0xffff0000, v52
	v_lshlrev_b32_e32 v118, 16, v53
	v_and_b32_e32 v119, 0xffff0000, v53
	v_lshlrev_b32_e32 v120, 16, v54
	v_and_b32_e32 v121, 0xffff0000, v54
	v_lshlrev_b32_e32 v122, 16, v55
	v_and_b32_e32 v123, 0xffff0000, v55
	v_lshlrev_b32_e32 v124, 16, v56
	v_and_b32_e32 v125, 0xffff0000, v56
	v_lshlrev_b32_e32 v126, 16, v57
	v_and_b32_e32 v127, 0xffff0000, v57
	v_lshlrev_b32_e32 v128, 16, v58
	v_and_b32_e32 v129, 0xffff0000, v58
	v_lshlrev_b32_e32 v130, 16, v59
	v_and_b32_e32 v131, 0xffff0000, v59
	v_pk_mul_f32 v[116:117], v[114:115], v[116:117] op_sel_hi:[0,1]
	v_pk_mul_f32 v[118:119], v[114:115], v[118:119] op_sel_hi:[0,1]
	v_pk_mul_f32 v[120:121], v[114:115], v[120:121] op_sel_hi:[0,1]
	v_pk_mul_f32 v[122:123], v[114:115], v[122:123] op_sel_hi:[0,1]
	v_pk_mul_f32 v[124:125], v[114:115], v[124:125] op_sel_hi:[0,1]
	v_pk_mul_f32 v[126:127], v[114:115], v[126:127] op_sel_hi:[0,1]
	v_pk_mul_f32 v[128:129], v[114:115], v[128:129] op_sel_hi:[0,1]
	v_pk_mul_f32 v[130:131], v[114:115], v[130:131] op_sel_hi:[0,1]
	v_pk_mul_f32 v[132:133], v[8:9], v[116:117]
	v_pk_mul_f32 v[134:135], v[10:11], v[118:119]
	v_pk_mul_f32 v[136:137], v[12:13], v[120:121]
	v_pk_mul_f32 v[138:139], v[14:15], v[122:123]
	v_pk_mul_f32 v[140:141], v[16:17], v[124:125]
	v_pk_mul_f32 v[142:143], v[18:19], v[126:127]
	v_pk_mul_f32 v[144:145], v[20:21], v[128:129]
	v_pk_mul_f32 v[146:147], v[22:23], v[130:131]
	global_store_dwordx4 v2, v[132:135], s[34:35]
	global_store_dwordx4 v2, v[136:139], s[34:35] offset:16
	global_store_dwordx4 v2, v[140:143], s[34:35] offset:2048
	global_store_dwordx4 v2, v[144:147], s[34:35] offset:2064
	s_waitcnt vmcnt(24)
	v_add_f32_dpp v112, v70, v70 quad_perm:[1,0,3,2] row_mask:0xf bank_mask:0xf
	s_mov_b64 s[36:37], s[24:25]
	s_add_u32 s24, s24, s22
	v_add_f32_dpp v112, v112, v112 quad_perm:[2,3,0,1] row_mask:0xf bank_mask:0xf
	s_addc_u32 s25, s25, 0
	s_nop 0
	v_add_f32_dpp v112, v112, v112 row_half_mirror row_mask:0xf bank_mask:0xf
	s_nop 1
	v_add_f32_dpp v112, v112, v112 row_mirror row_mask:0xf bank_mask:0xf
	v_fmamk_f32 v112, v112, 0x3a800000, v5
	v_rsq_f32_e32 v114, v112
	v_lshlrev_b32_e32 v116, 16, v62
	v_and_b32_e32 v117, 0xffff0000, v62
	v_lshlrev_b32_e32 v118, 16, v63
	v_and_b32_e32 v119, 0xffff0000, v63
	v_lshlrev_b32_e32 v120, 16, v64
	v_and_b32_e32 v121, 0xffff0000, v64
	v_lshlrev_b32_e32 v122, 16, v65
	v_and_b32_e32 v123, 0xffff0000, v65
	v_lshlrev_b32_e32 v124, 16, v66
	v_and_b32_e32 v125, 0xffff0000, v66
	v_lshlrev_b32_e32 v126, 16, v67
	v_and_b32_e32 v127, 0xffff0000, v67
	v_lshlrev_b32_e32 v128, 16, v68
	v_and_b32_e32 v129, 0xffff0000, v68
	v_lshlrev_b32_e32 v130, 16, v69
	v_and_b32_e32 v131, 0xffff0000, v69
	v_pk_mul_f32 v[116:117], v[114:115], v[116:117] op_sel_hi:[0,1]
	v_pk_mul_f32 v[118:119], v[114:115], v[118:119] op_sel_hi:[0,1]
	v_pk_mul_f32 v[120:121], v[114:115], v[120:121] op_sel_hi:[0,1]
	v_pk_mul_f32 v[122:123], v[114:115], v[122:123] op_sel_hi:[0,1]
	v_pk_mul_f32 v[124:125], v[114:115], v[124:125] op_sel_hi:[0,1]
	v_pk_mul_f32 v[126:127], v[114:115], v[126:127] op_sel_hi:[0,1]
	v_pk_mul_f32 v[128:129], v[114:115], v[128:129] op_sel_hi:[0,1]
	v_pk_mul_f32 v[130:131], v[114:115], v[130:131] op_sel_hi:[0,1]
	v_pk_mul_f32 v[132:133], v[8:9], v[116:117]
	v_pk_mul_f32 v[134:135], v[10:11], v[118:119]
	v_pk_mul_f32 v[136:137], v[12:13], v[120:121]
	v_pk_mul_f32 v[138:139], v[14:15], v[122:123]
	v_pk_mul_f32 v[140:141], v[16:17], v[124:125]
	v_pk_mul_f32 v[142:143], v[18:19], v[126:127]
	v_pk_mul_f32 v[144:145], v[20:21], v[128:129]
	v_pk_mul_f32 v[146:147], v[22:23], v[130:131]
	global_store_dwordx4 v2, v[132:135], s[36:37]
	global_store_dwordx4 v2, v[136:139], s[36:37] offset:16
	global_store_dwordx4 v2, v[140:143], s[36:37] offset:2048
	global_store_dwordx4 v2, v[144:147], s[36:37] offset:2064
.Lfin_loop:
	s_add_i32 s14, s12, s23
	s_cmp_lt_i32 s14, 0x10000
	s_cbranch_scc0 .Lfin_drain
	s_mov_b64 s[26:27], s[16:17]
	s_mov_b64 s[28:29], s[18:19]
	global_load_dword v40, v4, s[26:27]
	global_load_dwordx4 v[32:35], v3, s[28:29]
	global_load_dwordx4 v[36:39], v3, s[28:29] offset:1024
	s_add_u32 s16, s16, s20
	s_addc_u32 s17, s17, 0
	s_add_u32 s18, s18, s21
	s_addc_u32 s19, s19, 0
	s_add_i32 s12, s12, s13
	s_mov_b64 s[30:31], s[16:17]
	s_mov_b64 s[32:33], s[18:19]
	global_load_dword v50, v4, s[30:31]
	global_load_dwordx4 v[42:45], v3, s[32:33]
	global_load_dwordx4 v[46:49], v3, s[32:33] offset:1024
	s_add_u32 s16, s16, s20
	s_addc_u32 s17, s17, 0
	s_add_u32 s18, s18, s21
	s_addc_u32 s19, s19, 0
	s_add_i32 s12, s12, s13
	s_mov_b64 s[26:27], s[16:17]
	s_mov_b64 s[28:29], s[18:19]
	global_load_dword v60, v4, s[26:27]
	global_load_dwordx4 v[52:55], v3, s[28:29]
	global_load_dwordx4 v[56:59], v3, s[28:29] offset:1024
	s_add_u32 s16, s16, s20
	s_addc_u32 s17, s17, 0
	s_add_u32 s18, s18, s21
	s_addc_u32 s19, s19, 0
	s_add_i32 s12, s12, s13
	s_mov_b64 s[30:31], s[16:17]
	s_mov_b64 s[32:33], s[18:19]
	global_load_dword v70, v4, s[30:31]
	global_load_dwordx4 v[62:65], v3, s[32:33]
	global_load_dwordx4 v[66:69], v3, s[32:33] offset:1024
	s_add_u32 s16, s16, s20
	s_addc_u32 s17, s17, 0
	s_add_u32 s18, s18, s21
	s_addc_u32 s19, s19, 0
	s_add_i32 s12, s12, s13
	s_waitcnt vmcnt(37)
	v_add_f32_dpp v112, v80, v80 quad_perm:[1,0,3,2] row_mask:0xf bank_mask:0xf
	s_mov_b64 s[34:35], s[24:25]
	s_add_u32 s24, s24, s22
	v_add_f32_dpp v112, v112, v112 quad_perm:[2,3,0,1] row_mask:0xf bank_mask:0xf
	s_addc_u32 s25, s25, 0
	s_nop 0
	v_add_f32_dpp v112, v112, v112 row_half_mirror row_mask:0xf bank_mask:0xf
	s_nop 1
	v_add_f32_dpp v112, v112, v112 row_mirror row_mask:0xf bank_mask:0xf
	v_fmamk_f32 v112, v112, 0x3a800000, v5
	v_rsq_f32_e32 v114, v112
	v_lshlrev_b32_e32 v116, 16, v72
	v_and_b32_e32 v117, 0xffff0000, v72
	v_lshlrev_b32_e32 v118, 16, v73
	v_and_b32_e32 v119, 0xffff0000, v73
	v_lshlrev_b32_e32 v120, 16, v74
	v_and_b32_e32 v121, 0xffff0000, v74
	v_lshlrev_b32_e32 v122, 16, v75
	v_and_b32_e32 v123, 0xffff0000, v75
	v_lshlrev_b32_e32 v124, 16, v76
	v_and_b32_e32 v125, 0xffff0000, v76
	v_lshlrev_b32_e32 v126, 16, v77
	v_and_b32_e32 v127, 0xffff0000, v77
	v_lshlrev_b32_e32 v128, 16, v78
	v_and_b32_e32 v129, 0xffff0000, v78
	v_lshlrev_b32_e32 v130, 16, v79
	v_and_b32_e32 v131, 0xffff0000, v79
	v_pk_mul_f32 v[116:117], v[114:115], v[116:117] op_sel_hi:[0,1]
	v_pk_mul_f32 v[118:119], v[114:115], v[118:119] op_sel_hi:[0,1]
	v_pk_mul_f32 v[120:121], v[114:115], v[120:121] op_sel_hi:[0,1]
	v_pk_mul_f32 v[122:123], v[114:115], v[122:123] op_sel_hi:[0,1]
	v_pk_mul_f32 v[124:125], v[114:115], v[124:125] op_sel_hi:[0,1]
	v_pk_mul_f32 v[126:127], v[114:115], v[126:127] op_sel_hi:[0,1]
	v_pk_mul_f32 v[128:129], v[114:115], v[128:129] op_sel_hi:[0,1]
	v_pk_mul_f32 v[130:131], v[114:115], v[130:131] op_sel_hi:[0,1]
	v_pk_mul_f32 v[132:133], v[8:9], v[116:117]
	v_pk_mul_f32 v[134:135], v[10:11], v[118:119]
	v_pk_mul_f32 v[136:137], v[12:13], v[120:121]
	v_pk_mul_f32 v[138:139], v[14:15], v[122:123]
	v_pk_mul_f32 v[140:141], v[16:17], v[124:125]
	v_pk_mul_f32 v[142:143], v[18:19], v[126:127]
	v_pk_mul_f32 v[144:145], v[20:21], v[128:129]
	v_pk_mul_f32 v[146:147], v[22:23], v[130:131]
	global_store_dwordx4 v2, v[132:135], s[34:35]
	global_store_dwordx4 v2, v[136:139], s[34:35] offset:16
	global_store_dwordx4 v2, v[140:143], s[34:35] offset:2048
	global_store_dwordx4 v2, v[144:147], s[34:35] offset:2064
	s_waitcnt vmcnt(38)
	v_add_f32_dpp v112, v90, v90 quad_perm:[1,0,3,2] row_mask:0xf bank_mask:0xf
	s_mov_b64 s[36:37], s[24:25]
	s_add_u32 s24, s24, s22
	v_add_f32_dpp v112, v112, v112 quad_perm:[2,3,0,1] row_mask:0xf bank_mask:0xf
	s_addc_u32 s25, s25, 0
	s_nop 0
	v_add_f32_dpp v112, v112, v112 row_half_mirror row_mask:0xf bank_mask:0xf
	s_nop 1
	v_add_f32_dpp v112, v112, v112 row_mirror row_mask:0xf bank_mask:0xf
	v_fmamk_f32 v112, v112, 0x3a800000, v5
	v_rsq_f32_e32 v114, v112
	v_lshlrev_b32_e32 v116, 16, v82
	v_and_b32_e32 v117, 0xffff0000, v82
	v_lshlrev_b32_e32 v118, 16, v83
	v_and_b32_e32 v119, 0xffff0000, v83
	v_lshlrev_b32_e32 v120, 16, v84
	v_and_b32_e32 v121, 0xffff0000, v84
	v_lshlrev_b32_e32 v122, 16, v85
	v_and_b32_e32 v123, 0xffff0000, v85
	v_lshlrev_b32_e32 v124, 16, v86
	v_and_b32_e32 v125, 0xffff0000, v86
	v_lshlrev_b32_e32 v126, 16, v87
	v_and_b32_e32 v127, 0xffff0000, v87
	v_lshlrev_b32_e32 v128, 16, v88
	v_and_b32_e32 v129, 0xffff0000, v88
	v_lshlrev_b32_e32 v130, 16, v89
	v_and_b32_e32 v131, 0xffff0000, v89
	v_pk_mul_f32 v[116:117], v[114:115], v[116:117] op_sel_hi:[0,1]
	v_pk_mul_f32 v[118:119], v[114:115], v[118:119] op_sel_hi:[0,1]
	v_pk_mul_f32 v[120:121], v[114:115], v[120:121] op_sel_hi:[0,1]
	v_pk_mul_f32 v[122:123], v[114:115], v[122:123] op_sel_hi:[0,1]
	v_pk_mul_f32 v[124:125], v[114:115], v[124:125] op_sel_hi:[0,1]
	v_pk_mul_f32 v[126:127], v[114:115], v[126:127] op_sel_hi:[0,1]
	v_pk_mul_f32 v[128:129], v[114:115], v[128:129] op_sel_hi:[0,1]
	v_pk_mul_f32 v[130:131], v[114:115], v[130:131] op_sel_hi:[0,1]
	v_pk_mul_f32 v[132:133], v[8:9], v[116:117]
	v_pk_mul_f32 v[134:135], v[10:11], v[118:119]
	v_pk_mul_f32 v[136:137], v[12:13], v[120:121]
	v_pk_mul_f32 v[138:139], v[14:15], v[122:123]
	v_pk_mul_f32 v[140:141], v[16:17], v[124:125]
	v_pk_mul_f32 v[142:143], v[18:19], v[126:127]
	v_pk_mul_f32 v[144:145], v[20:21], v[128:129]
	v_pk_mul_f32 v[146:147], v[22:23], v[130:131]
	global_store_dwordx4 v2, v[132:135], s[36:37]
	global_store_dwordx4 v2, v[136:139], s[36:37] offset:16
	global_store_dwordx4 v2, v[140:143], s[36:37] offset:2048
	global_store_dwordx4 v2, v[144:147], s[36:37] offset:2064
	s_waitcnt vmcnt(39)
	v_add_f32_dpp v112, v100, v100 quad_perm:[1,0,3,2] row_mask:0xf bank_mask:0xf
	s_mov_b64 s[34:35], s[24:25]
	s_add_u32 s24, s24, s22
	v_add_f32_dpp v112, v112, v112 quad_perm:[2,3,0,1] row_mask:0xf bank_mask:0xf
	s_addc_u32 s25, s25, 0
	s_nop 0
	v_add_f32_dpp v112, v112, v112 row_half_mirror row_mask:0xf bank_mask:0xf
	s_nop 1
	v_add_f32_dpp v112, v112, v112 row_mirror row_mask:0xf bank_mask:0xf
	v_fmamk_f32 v112, v112, 0x3a800000, v5
	v_rsq_f32_e32 v114, v112
	v_lshlrev_b32_e32 v116, 16, v92
	v_and_b32_e32 v117, 0xffff0000, v92
	v_lshlrev_b32_e32 v118, 16, v93
	v_and_b32_e32 v119, 0xffff0000, v93
	v_lshlrev_b32_e32 v120, 16, v94
	v_and_b32_e32 v121, 0xffff0000, v94
	v_lshlrev_b32_e32 v122, 16, v95
	v_and_b32_e32 v123, 0xffff0000, v95
	v_lshlrev_b32_e32 v124, 16, v96
	v_and_b32_e32 v125, 0xffff0000, v96
	v_lshlrev_b32_e32 v126, 16, v97
	v_and_b32_e32 v127, 0xffff0000, v97
	v_lshlrev_b32_e32 v128, 16, v98
	v_and_b32_e32 v129, 0xffff0000, v98
	v_lshlrev_b32_e32 v130, 16, v99
	v_and_b32_e32 v131, 0xffff0000, v99
	v_pk_mul_f32 v[116:117], v[114:115], v[116:117] op_sel_hi:[0,1]
	v_pk_mul_f32 v[118:119], v[114:115], v[118:119] op_sel_hi:[0,1]
	v_pk_mul_f32 v[120:121], v[114:115], v[120:121] op_sel_hi:[0,1]
	v_pk_mul_f32 v[122:123], v[114:115], v[122:123] op_sel_hi:[0,1]
	v_pk_mul_f32 v[124:125], v[114:115], v[124:125] op_sel_hi:[0,1]
	v_pk_mul_f32 v[126:127], v[114:115], v[126:127] op_sel_hi:[0,1]
	v_pk_mul_f32 v[128:129], v[114:115], v[128:129] op_sel_hi:[0,1]
	v_pk_mul_f32 v[130:131], v[114:115], v[130:131] op_sel_hi:[0,1]
	v_pk_mul_f32 v[132:133], v[8:9], v[116:117]
	v_pk_mul_f32 v[134:135], v[10:11], v[118:119]
	v_pk_mul_f32 v[136:137], v[12:13], v[120:121]
	v_pk_mul_f32 v[138:139], v[14:15], v[122:123]
	v_pk_mul_f32 v[140:141], v[16:17], v[124:125]
	v_pk_mul_f32 v[142:143], v[18:19], v[126:127]
	v_pk_mul_f32 v[144:145], v[20:21], v[128:129]
	v_pk_mul_f32 v[146:147], v[22:23], v[130:131]
	global_store_dwordx4 v2, v[132:135], s[34:35]
	global_store_dwordx4 v2, v[136:139], s[34:35] offset:16
	global_store_dwordx4 v2, v[140:143], s[34:35] offset:2048
	global_store_dwordx4 v2, v[144:147], s[34:35] offset:2064
	s_waitcnt vmcnt(40)
	v_add_f32_dpp v112, v110, v110 quad_perm:[1,0,3,2] row_mask:0xf bank_mask:0xf
	s_mov_b64 s[36:37], s[24:25]
	s_add_u32 s24, s24, s22
	v_add_f32_dpp v112, v112, v112 quad_perm:[2,3,0,1] row_mask:0xf bank_mask:0xf
	s_addc_u32 s25, s25, 0
	s_nop 0
	v_add_f32_dpp v112, v112, v112 row_half_mirror row_mask:0xf bank_mask:0xf
	s_nop 1
	v_add_f32_dpp v112, v112, v112 row_mirror row_mask:0xf bank_mask:0xf
	v_fmamk_f32 v112, v112, 0x3a800000, v5
	v_rsq_f32_e32 v114, v112
	v_lshlrev_b32_e32 v116, 16, v102
	v_and_b32_e32 v117, 0xffff0000, v102
	v_lshlrev_b32_e32 v118, 16, v103
	v_and_b32_e32 v119, 0xffff0000, v103
	v_lshlrev_b32_e32 v120, 16, v104
	v_and_b32_e32 v121, 0xffff0000, v104
	v_lshlrev_b32_e32 v122, 16, v105
	v_and_b32_e32 v123, 0xffff0000, v105
	v_lshlrev_b32_e32 v124, 16, v106
	v_and_b32_e32 v125, 0xffff0000, v106
	v_lshlrev_b32_e32 v126, 16, v107
	v_and_b32_e32 v127, 0xffff0000, v107
	v_lshlrev_b32_e32 v128, 16, v108
	v_and_b32_e32 v129, 0xffff0000, v108
	v_lshlrev_b32_e32 v130, 16, v109
	v_and_b32_e32 v131, 0xffff0000, v109
	v_pk_mul_f32 v[116:117], v[114:115], v[116:117] op_sel_hi:[0,1]
	v_pk_mul_f32 v[118:119], v[114:115], v[118:119] op_sel_hi:[0,1]
	v_pk_mul_f32 v[120:121], v[114:115], v[120:121] op_sel_hi:[0,1]
	v_pk_mul_f32 v[122:123], v[114:115], v[122:123] op_sel_hi:[0,1]
	v_pk_mul_f32 v[124:125], v[114:115], v[124:125] op_sel_hi:[0,1]
	v_pk_mul_f32 v[126:127], v[114:115], v[126:127] op_sel_hi:[0,1]
	v_pk_mul_f32 v[128:129], v[114:115], v[128:129] op_sel_hi:[0,1]
	v_pk_mul_f32 v[130:131], v[114:115], v[130:131] op_sel_hi:[0,1]
	v_pk_mul_f32 v[132:133], v[8:9], v[116:117]
	v_pk_mul_f32 v[134:135], v[10:11], v[118:119]
	v_pk_mul_f32 v[136:137], v[12:13], v[120:121]
	v_pk_mul_f32 v[138:139], v[14:15], v[122:123]
	v_pk_mul_f32 v[140:141], v[16:17], v[124:125]
	v_pk_mul_f32 v[142:143], v[18:19], v[126:127]
	v_pk_mul_f32 v[144:145], v[20:21], v[128:129]
	v_pk_mul_f32 v[146:147], v[22:23], v[130:131]
	global_store_dwordx4 v2, v[132:135], s[36:37]
	global_store_dwordx4 v2, v[136:139], s[36:37] offset:16
	global_store_dwordx4 v2, v[140:143], s[36:37] offset:2048
	global_store_dwordx4 v2, v[144:147], s[36:37] offset:2064
	s_mov_b64 s[26:27], s[16:17]
	s_mov_b64 s[28:29], s[18:19]
	global_load_dword v80, v4, s[26:27]
	global_load_dwordx4 v[72:75], v3, s[28:29]
	global_load_dwordx4 v[76:79], v3, s[28:29] offset:1024
	s_add_u32 s16, s16, s20
	s_addc_u32 s17, s17, 0
	s_add_u32 s18, s18, s21
	s_addc_u32 s19, s19, 0
	s_add_i32 s12, s12, s13
	s_mov_b64 s[30:31], s[16:17]
	s_mov_b64 s[32:33], s[18:19]
	global_load_dword v90, v4, s[30:31]
	global_load_dwordx4 v[82:85], v3, s[32:33]
	global_load_dwordx4 v[86:89], v3, s[32:33] offset:1024
	s_add_u32 s16, s16, s20
	s_addc_u32 s17, s17, 0
	s_add_u32 s18, s18, s21
	s_addc_u32 s19, s19, 0
	s_add_i32 s12, s12, s13
	s_mov_b64 s[26:27], s[16:17]
	s_mov_b64 s[28:29], s[18:19]
	global_load_dword v100, v4, s[26:27]
	global_load_dwordx4 v[92:95], v3, s[28:29]
	global_load_dwordx4 v[96:99], v3, s[28:29] offset:1024
	s_add_u32 s16, s16, s20
	s_addc_u32 s17, s17, 0
	s_add_u32 s18, s18, s21
	s_addc_u32 s19, s19, 0
	s_add_i32 s12, s12, s13
	s_mov_b64 s[30:31], s[16:17]
	s_mov_b64 s[32:33], s[18:19]
	global_load_dword v110, v4, s[30:31]
	global_load_dwordx4 v[102:105], v3, s[32:33]
	global_load_dwordx4 v[106:109], v3, s[32:33] offset:1024
	s_add_u32 s16, s16, s20
	s_addc_u32 s17, s17, 0
	s_add_u32 s18, s18, s21
	s_addc_u32 s19, s19, 0
	s_add_i32 s12, s12, s13
	s_waitcnt vmcnt(37)
	v_add_f32_dpp v112, v40, v40 quad_perm:[1,0,3,2] row_mask:0xf bank_mask:0xf
	s_mov_b64 s[34:35], s[24:25]
	s_add_u32 s24, s24, s22
	v_add_f32_dpp v112, v112, v112 quad_perm:[2,3,0,1] row_mask:0xf bank_mask:0xf
	s_addc_u32 s25, s25, 0
	s_nop 0
	v_add_f32_dpp v112, v112, v112 row_half_mirror row_mask:0xf bank_mask:0xf
	s_nop 1
	v_add_f32_dpp v112, v112, v112 row_mirror row_mask:0xf bank_mask:0xf
	v_fmamk_f32 v112, v112, 0x3a800000, v5
	v_rsq_f32_e32 v114, v112
	v_lshlrev_b32_e32 v116, 16, v32
	v_and_b32_e32 v117, 0xffff0000, v32
	v_lshlrev_b32_e32 v118, 16, v33
	v_and_b32_e32 v119, 0xffff0000, v33
	v_lshlrev_b32_e32 v120, 16, v34
	v_and_b32_e32 v121, 0xffff0000, v34
	v_lshlrev_b32_e32 v122, 16, v35
	v_and_b32_e32 v123, 0xffff0000, v35
	v_lshlrev_b32_e32 v124, 16, v36
	v_and_b32_e32 v125, 0xffff0000, v36
	v_lshlrev_b32_e32 v126, 16, v37
	v_and_b32_e32 v127, 0xffff0000, v37
	v_lshlrev_b32_e32 v128, 16, v38
	v_and_b32_e32 v129, 0xffff0000, v38
	v_lshlrev_b32_e32 v130, 16, v39
	v_and_b32_e32 v131, 0xffff0000, v39
	v_pk_mul_f32 v[116:117], v[114:115], v[116:117] op_sel_hi:[0,1]
	v_pk_mul_f32 v[118:119], v[114:115], v[118:119] op_sel_hi:[0,1]
	v_pk_mul_f32 v[120:121], v[114:115], v[120:121] op_sel_hi:[0,1]
	v_pk_mul_f32 v[122:123], v[114:115], v[122:123] op_sel_hi:[0,1]
	v_pk_mul_f32 v[124:125], v[114:115], v[124:125] op_sel_hi:[0,1]
	v_pk_mul_f32 v[126:127], v[114:115], v[126:127] op_sel_hi:[0,1]
	v_pk_mul_f32 v[128:129], v[114:115], v[128:129] op_sel_hi:[0,1]
	v_pk_mul_f32 v[130:131], v[114:115], v[130:131] op_sel_hi:[0,1]
	v_pk_mul_f32 v[132:133], v[8:9], v[116:117]
	v_pk_mul_f32 v[134:135], v[10:11], v[118:119]
	v_pk_mul_f32 v[136:137], v[12:13], v[120:121]
	v_pk_mul_f32 v[138:139], v[14:15], v[122:123]
	v_pk_mul_f32 v[140:141], v[16:17], v[124:125]
	v_pk_mul_f32 v[142:143], v[18:19], v[126:127]
	v_pk_mul_f32 v[144:145], v[20:21], v[128:129]
	v_pk_mul_f32 v[146:147], v[22:23], v[130:131]
	global_store_dwordx4 v2, v[132:135], s[34:35]
	global_store_dwordx4 v2, v[136:139], s[34:35] offset:16
	global_store_dwordx4 v2, v[140:143], s[34:35] offset:2048
	global_store_dwordx4 v2, v[144:147], s[34:35] offset:2064
	s_waitcnt vmcnt(38)
	v_add_f32_dpp v112, v50, v50 quad_perm:[1,0,3,2] row_mask:0xf bank_mask:0xf
	s_mov_b64 s[36:37], s[24:25]
	s_add_u32 s24, s24, s22
	v_add_f32_dpp v112, v112, v112 quad_perm:[2,3,0,1] row_mask:0xf bank_mask:0xf
	s_addc_u32 s25, s25, 0
	s_nop 0
	v_add_f32_dpp v112, v112, v112 row_half_mirror row_mask:0xf bank_mask:0xf
	s_nop 1
	v_add_f32_dpp v112, v112, v112 row_mirror row_mask:0xf bank_mask:0xf
	v_fmamk_f32 v112, v112, 0x3a800000, v5
	v_rsq_f32_e32 v114, v112
	v_lshlrev_b32_e32 v116, 16, v42
	v_and_b32_e32 v117, 0xffff0000, v42
	v_lshlrev_b32_e32 v118, 16, v43
	v_and_b32_e32 v119, 0xffff0000, v43
	v_lshlrev_b32_e32 v120, 16, v44
	v_and_b32_e32 v121, 0xffff0000, v44
	v_lshlrev_b32_e32 v122, 16, v45
	v_and_b32_e32 v123, 0xffff0000, v45
	v_lshlrev_b32_e32 v124, 16, v46
	v_and_b32_e32 v125, 0xffff0000, v46
	v_lshlrev_b32_e32 v126, 16, v47
	v_and_b32_e32 v127, 0xffff0000, v47
	v_lshlrev_b32_e32 v128, 16, v48
	v_and_b32_e32 v129, 0xffff0000, v48
	v_lshlrev_b32_e32 v130, 16, v49
	v_and_b32_e32 v131, 0xffff0000, v49
	v_pk_mul_f32 v[116:117], v[114:115], v[116:117] op_sel_hi:[0,1]
	v_pk_mul_f32 v[118:119], v[114:115], v[118:119] op_sel_hi:[0,1]
	v_pk_mul_f32 v[120:121], v[114:115], v[120:121] op_sel_hi:[0,1]
	v_pk_mul_f32 v[122:123], v[114:115], v[122:123] op_sel_hi:[0,1]
	v_pk_mul_f32 v[124:125], v[114:115], v[124:125] op_sel_hi:[0,1]
	v_pk_mul_f32 v[126:127], v[114:115], v[126:127] op_sel_hi:[0,1]
	v_pk_mul_f32 v[128:129], v[114:115], v[128:129] op_sel_hi:[0,1]
	v_pk_mul_f32 v[130:131], v[114:115], v[130:131] op_sel_hi:[0,1]
	v_pk_mul_f32 v[132:133], v[8:9], v[116:117]
	v_pk_mul_f32 v[134:135], v[10:11], v[118:119]
	v_pk_mul_f32 v[136:137], v[12:13], v[120:121]
	v_pk_mul_f32 v[138:139], v[14:15], v[122:123]
	v_pk_mul_f32 v[140:141], v[16:17], v[124:125]
	v_pk_mul_f32 v[142:143], v[18:19], v[126:127]
	v_pk_mul_f32 v[144:145], v[20:21], v[128:129]
	v_pk_mul_f32 v[146:147], v[22:23], v[130:131]
	global_store_dwordx4 v2, v[132:135], s[36:37]
	global_store_dwordx4 v2, v[136:139], s[36:37] offset:16
	global_store_dwordx4 v2, v[140:143], s[36:37] offset:2048
	global_store_dwordx4 v2, v[144:147], s[36:37] offset:2064
	s_waitcnt vmcnt(39)
	v_add_f32_dpp v112, v60, v60 quad_perm:[1,0,3,2] row_mask:0xf bank_mask:0xf
	s_mov_b64 s[34:35], s[24:25]
	s_add_u32 s24, s24, s22
	v_add_f32_dpp v112, v112, v112 quad_perm:[2,3,0,1] row_mask:0xf bank_mask:0xf
	s_addc_u32 s25, s25, 0
	s_nop 0
	v_add_f32_dpp v112, v112, v112 row_half_mirror row_mask:0xf bank_mask:0xf
	s_nop 1
	v_add_f32_dpp v112, v112, v112 row_mirror row_mask:0xf bank_mask:0xf
	v_fmamk_f32 v112, v112, 0x3a800000, v5
	v_rsq_f32_e32 v114, v112
	v_lshlrev_b32_e32 v116, 16, v52
	v_and_b32_e32 v117, 0xffff0000, v52
	v_lshlrev_b32_e32 v118, 16, v53
	v_and_b32_e32 v119, 0xffff0000, v53
	v_lshlrev_b32_e32 v120, 16, v54
	v_and_b32_e32 v121, 0xffff0000, v54
	v_lshlrev_b32_e32 v122, 16, v55
	v_and_b32_e32 v123, 0xffff0000, v55
	v_lshlrev_b32_e32 v124, 16, v56
	v_and_b32_e32 v125, 0xffff0000, v56
	v_lshlrev_b32_e32 v126, 16, v57
	v_and_b32_e32 v127, 0xffff0000, v57
	v_lshlrev_b32_e32 v128, 16, v58
	v_and_b32_e32 v129, 0xffff0000, v58
	v_lshlrev_b32_e32 v130, 16, v59
	v_and_b32_e32 v131, 0xffff0000, v59
	v_pk_mul_f32 v[116:117], v[114:115], v[116:117] op_sel_hi:[0,1]
	v_pk_mul_f32 v[118:119], v[114:115], v[118:119] op_sel_hi:[0,1]
	v_pk_mul_f32 v[120:121], v[114:115], v[120:121] op_sel_hi:[0,1]
	v_pk_mul_f32 v[122:123], v[114:115], v[122:123] op_sel_hi:[0,1]
	v_pk_mul_f32 v[124:125], v[114:115], v[124:125] op_sel_hi:[0,1]
	v_pk_mul_f32 v[126:127], v[114:115], v[126:127] op_sel_hi:[0,1]
	v_pk_mul_f32 v[128:129], v[114:115], v[128:129] op_sel_hi:[0,1]
	v_pk_mul_f32 v[130:131], v[114:115], v[130:131] op_sel_hi:[0,1]
	v_pk_mul_f32 v[132:133], v[8:9], v[116:117]
	v_pk_mul_f32 v[134:135], v[10:11], v[118:119]
	v_pk_mul_f32 v[136:137], v[12:13], v[120:121]
	v_pk_mul_f32 v[138:139], v[14:15], v[122:123]
	v_pk_mul_f32 v[140:141], v[16:17], v[124:125]
	v_pk_mul_f32 v[142:143], v[18:19], v[126:127]
	v_pk_mul_f32 v[144:145], v[20:21], v[128:129]
	v_pk_mul_f32 v[146:147], v[22:23], v[130:131]
	global_store_dwordx4 v2, v[132:135], s[34:35]
	global_store_dwordx4 v2, v[136:139], s[34:35] offset:16
	global_store_dwordx4 v2, v[140:143], s[34:35] offset:2048
	global_store_dwordx4 v2, v[144:147], s[34:35] offset:2064
	s_waitcnt vmcnt(40)
	v_add_f32_dpp v112, v70, v70 quad_perm:[1,0,3,2] row_mask:0xf bank_mask:0xf
	s_mov_b64 s[36:37], s[24:25]
	s_add_u32 s24, s24, s22
	v_add_f32_dpp v112, v112, v112 quad_perm:[2,3,0,1] row_mask:0xf bank_mask:0xf
	s_addc_u32 s25, s25, 0
	s_nop 0
	v_add_f32_dpp v112, v112, v112 row_half_mirror row_mask:0xf bank_mask:0xf
	s_nop 1
	v_add_f32_dpp v112, v112, v112 row_mirror row_mask:0xf bank_mask:0xf
	v_fmamk_f32 v112, v112, 0x3a800000, v5
	v_rsq_f32_e32 v114, v112
	v_lshlrev_b32_e32 v116, 16, v62
	v_and_b32_e32 v117, 0xffff0000, v62
	v_lshlrev_b32_e32 v118, 16, v63
	v_and_b32_e32 v119, 0xffff0000, v63
	v_lshlrev_b32_e32 v120, 16, v64
	v_and_b32_e32 v121, 0xffff0000, v64
	v_lshlrev_b32_e32 v122, 16, v65
	v_and_b32_e32 v123, 0xffff0000, v65
	v_lshlrev_b32_e32 v124, 16, v66
	v_and_b32_e32 v125, 0xffff0000, v66
	v_lshlrev_b32_e32 v126, 16, v67
	v_and_b32_e32 v127, 0xffff0000, v67
	v_lshlrev_b32_e32 v128, 16, v68
	v_and_b32_e32 v129, 0xffff0000, v68
	v_lshlrev_b32_e32 v130, 16, v69
	v_and_b32_e32 v131, 0xffff0000, v69
	v_pk_mul_f32 v[116:117], v[114:115], v[116:117] op_sel_hi:[0,1]
	v_pk_mul_f32 v[118:119], v[114:115], v[118:119] op_sel_hi:[0,1]
	v_pk_mul_f32 v[120:121], v[114:115], v[120:121] op_sel_hi:[0,1]
	v_pk_mul_f32 v[122:123], v[114:115], v[122:123] op_sel_hi:[0,1]
	v_pk_mul_f32 v[124:125], v[114:115], v[124:125] op_sel_hi:[0,1]
	v_pk_mul_f32 v[126:127], v[114:115], v[126:127] op_sel_hi:[0,1]
	v_pk_mul_f32 v[128:129], v[114:115], v[128:129] op_sel_hi:[0,1]
	v_pk_mul_f32 v[130:131], v[114:115], v[130:131] op_sel_hi:[0,1]
	v_pk_mul_f32 v[132:133], v[8:9], v[116:117]
	v_pk_mul_f32 v[134:135], v[10:11], v[118:119]
	v_pk_mul_f32 v[136:137], v[12:13], v[120:121]
	v_pk_mul_f32 v[138:139], v[14:15], v[122:123]
	v_pk_mul_f32 v[140:141], v[16:17], v[124:125]
	v_pk_mul_f32 v[142:143], v[18:19], v[126:127]
	v_pk_mul_f32 v[144:145], v[20:21], v[128:129]
	v_pk_mul_f32 v[146:147], v[22:23], v[130:131]
	global_store_dwordx4 v2, v[132:135], s[36:37]
	global_store_dwordx4 v2, v[136:139], s[36:37] offset:16
	global_store_dwordx4 v2, v[140:143], s[36:37] offset:2048
	global_store_dwordx4 v2, v[144:147], s[36:37] offset:2064
	s_branch .Lfin_loop
.Lfin_drain:
	s_waitcnt vmcnt(25)
	v_add_f32_dpp v112, v80, v80 quad_perm:[1,0,3,2] row_mask:0xf bank_mask:0xf
	s_mov_b64 s[34:35], s[24:25]
	s_add_u32 s24, s24, s22
	v_add_f32_dpp v112, v112, v112 quad_perm:[2,3,0,1] row_mask:0xf bank_mask:0xf
	s_addc_u32 s25, s25, 0
	s_nop 0
	v_add_f32_dpp v112, v112, v112 row_half_mirror row_mask:0xf bank_mask:0xf
	s_nop 1
	v_add_f32_dpp v112, v112, v112 row_mirror row_mask:0xf bank_mask:0xf
	v_fmamk_f32 v112, v112, 0x3a800000, v5
	v_rsq_f32_e32 v114, v112
	v_lshlrev_b32_e32 v116, 16, v72
	v_and_b32_e32 v117, 0xffff0000, v72
	v_lshlrev_b32_e32 v118, 16, v73
	v_and_b32_e32 v119, 0xffff0000, v73
	v_lshlrev_b32_e32 v120, 16, v74
	v_and_b32_e32 v121, 0xffff0000, v74
	v_lshlrev_b32_e32 v122, 16, v75
	v_and_b32_e32 v123, 0xffff0000, v75
	v_lshlrev_b32_e32 v124, 16, v76
	v_and_b32_e32 v125, 0xffff0000, v76
	v_lshlrev_b32_e32 v126, 16, v77
	v_and_b32_e32 v127, 0xffff0000, v77
	v_lshlrev_b32_e32 v128, 16, v78
	v_and_b32_e32 v129, 0xffff0000, v78
	v_lshlrev_b32_e32 v130, 16, v79
	v_and_b32_e32 v131, 0xffff0000, v79
	v_pk_mul_f32 v[116:117], v[114:115], v[116:117] op_sel_hi:[0,1]
	v_pk_mul_f32 v[118:119], v[114:115], v[118:119] op_sel_hi:[0,1]
	v_pk_mul_f32 v[120:121], v[114:115], v[120:121] op_sel_hi:[0,1]
	v_pk_mul_f32 v[122:123], v[114:115], v[122:123] op_sel_hi:[0,1]
	v_pk_mul_f32 v[124:125], v[114:115], v[124:125] op_sel_hi:[0,1]
	v_pk_mul_f32 v[126:127], v[114:115], v[126:127] op_sel_hi:[0,1]
	v_pk_mul_f32 v[128:129], v[114:115], v[128:129] op_sel_hi:[0,1]
	v_pk_mul_f32 v[130:131], v[114:115], v[130:131] op_sel_hi:[0,1]
	v_pk_mul_f32 v[132:133], v[8:9], v[116:117]
	v_pk_mul_f32 v[134:135], v[10:11], v[118:119]
	v_pk_mul_f32 v[136:137], v[12:13], v[120:121]
	v_pk_mul_f32 v[138:139], v[14:15], v[122:123]
	v_pk_mul_f32 v[140:141], v[16:17], v[124:125]
	v_pk_mul_f32 v[142:143], v[18:19], v[126:127]
	v_pk_mul_f32 v[144:145], v[20:21], v[128:129]
	v_pk_mul_f32 v[146:147], v[22:23], v[130:131]
	global_store_dwordx4 v2, v[132:135], s[34:35]
	global_store_dwordx4 v2, v[136:139], s[34:35] offset:16
	global_store_dwordx4 v2, v[140:143], s[34:35] offset:2048
	global_store_dwordx4 v2, v[144:147], s[34:35] offset:2064
	s_waitcnt vmcnt(26)
	v_add_f32_dpp v112, v90, v90 quad_perm:[1,0,3,2] row_mask:0xf bank_mask:0xf
	s_mov_b64 s[36:37], s[24:25]
	s_add_u32 s24, s24, s22
	v_add_f32_dpp v112, v112, v112 quad_perm:[2,3,0,1] row_mask:0xf bank_mask:0xf
	s_addc_u32 s25, s25, 0
	s_nop 0
	v_add_f32_dpp v112, v112, v112 row_half_mirror row_mask:0xf bank_mask:0xf
	s_nop 1
	v_add_f32_dpp v112, v112, v112 row_mirror row_mask:0xf bank_mask:0xf
	v_fmamk_f32 v112, v112, 0x3a800000, v5
	v_rsq_f32_e32 v114, v112
	v_lshlrev_b32_e32 v116, 16, v82
	v_and_b32_e32 v117, 0xffff0000, v82
	v_lshlrev_b32_e32 v118, 16, v83
	v_and_b32_e32 v119, 0xffff0000, v83
	v_lshlrev_b32_e32 v120, 16, v84
	v_and_b32_e32 v121, 0xffff0000, v84
	v_lshlrev_b32_e32 v122, 16, v85
	v_and_b32_e32 v123, 0xffff0000, v85
	v_lshlrev_b32_e32 v124, 16, v86
	v_and_b32_e32 v125, 0xffff0000, v86
	v_lshlrev_b32_e32 v126, 16, v87
	v_and_b32_e32 v127, 0xffff0000, v87
	v_lshlrev_b32_e32 v128, 16, v88
	v_and_b32_e32 v129, 0xffff0000, v88
	v_lshlrev_b32_e32 v130, 16, v89
	v_and_b32_e32 v131, 0xffff0000, v89
	v_pk_mul_f32 v[116:117], v[114:115], v[116:117] op_sel_hi:[0,1]
	v_pk_mul_f32 v[118:119], v[114:115], v[118:119] op_sel_hi:[0,1]
	v_pk_mul_f32 v[120:121], v[114:115], v[120:121] op_sel_hi:[0,1]
	v_pk_mul_f32 v[122:123], v[114:115], v[122:123] op_sel_hi:[0,1]
	v_pk_mul_f32 v[124:125], v[114:115], v[124:125] op_sel_hi:[0,1]
	v_pk_mul_f32 v[126:127], v[114:115], v[126:127] op_sel_hi:[0,1]
	v_pk_mul_f32 v[128:129], v[114:115], v[128:129] op_sel_hi:[0,1]
	v_pk_mul_f32 v[130:131], v[114:115], v[130:131] op_sel_hi:[0,1]
	v_pk_mul_f32 v[132:133], v[8:9], v[116:117]
	v_pk_mul_f32 v[134:135], v[10:11], v[118:119]
	v_pk_mul_f32 v[136:137], v[12:13], v[120:121]
	v_pk_mul_f32 v[138:139], v[14:15], v[122:123]
	v_pk_mul_f32 v[140:141], v[16:17], v[124:125]
	v_pk_mul_f32 v[142:143], v[18:19], v[126:127]
	v_pk_mul_f32 v[144:145], v[20:21], v[128:129]
	v_pk_mul_f32 v[146:147], v[22:23], v[130:131]
	global_store_dwordx4 v2, v[132:135], s[36:37]
	global_store_dwordx4 v2, v[136:139], s[36:37] offset:16
	global_store_dwordx4 v2, v[140:143], s[36:37] offset:2048
	global_store_dwordx4 v2, v[144:147], s[36:37] offset:2064
	s_waitcnt vmcnt(27)
	v_add_f32_dpp v112, v100, v100 quad_perm:[1,0,3,2] row_mask:0xf bank_mask:0xf
	s_mov_b64 s[34:35], s[24:25]
	s_add_u32 s24, s24, s22
	v_add_f32_dpp v112, v112, v112 quad_perm:[2,3,0,1] row_mask:0xf bank_mask:0xf
	s_addc_u32 s25, s25, 0
	s_nop 0
	v_add_f32_dpp v112, v112, v112 row_half_mirror row_mask:0xf bank_mask:0xf
	s_nop 1
	v_add_f32_dpp v112, v112, v112 row_mirror row_mask:0xf bank_mask:0xf
	v_fmamk_f32 v112, v112, 0x3a800000, v5
	v_rsq_f32_e32 v114, v112
	v_lshlrev_b32_e32 v116, 16, v92
	v_and_b32_e32 v117, 0xffff0000, v92
	v_lshlrev_b32_e32 v118, 16, v93
	v_and_b32_e32 v119, 0xffff0000, v93
	v_lshlrev_b32_e32 v120, 16, v94
	v_and_b32_e32 v121, 0xffff0000, v94
	v_lshlrev_b32_e32 v122, 16, v95
	v_and_b32_e32 v123, 0xffff0000, v95
	v_lshlrev_b32_e32 v124, 16, v96
	v_and_b32_e32 v125, 0xffff0000, v96
	v_lshlrev_b32_e32 v126, 16, v97
	v_and_b32_e32 v127, 0xffff0000, v97
	v_lshlrev_b32_e32 v128, 16, v98
	v_and_b32_e32 v129, 0xffff0000, v98
	v_lshlrev_b32_e32 v130, 16, v99
	v_and_b32_e32 v131, 0xffff0000, v99
	v_pk_mul_f32 v[116:117], v[114:115], v[116:117] op_sel_hi:[0,1]
	v_pk_mul_f32 v[118:119], v[114:115], v[118:119] op_sel_hi:[0,1]
	v_pk_mul_f32 v[120:121], v[114:115], v[120:121] op_sel_hi:[0,1]
	v_pk_mul_f32 v[122:123], v[114:115], v[122:123] op_sel_hi:[0,1]
	v_pk_mul_f32 v[124:125], v[114:115], v[124:125] op_sel_hi:[0,1]
	v_pk_mul_f32 v[126:127], v[114:115], v[126:127] op_sel_hi:[0,1]
	v_pk_mul_f32 v[128:129], v[114:115], v[128:129] op_sel_hi:[0,1]
	v_pk_mul_f32 v[130:131], v[114:115], v[130:131] op_sel_hi:[0,1]
	v_pk_mul_f32 v[132:133], v[8:9], v[116:117]
	v_pk_mul_f32 v[134:135], v[10:11], v[118:119]
	v_pk_mul_f32 v[136:137], v[12:13], v[120:121]
	v_pk_mul_f32 v[138:139], v[14:15], v[122:123]
	v_pk_mul_f32 v[140:141], v[16:17], v[124:125]
	v_pk_mul_f32 v[142:143], v[18:19], v[126:127]
	v_pk_mul_f32 v[144:145], v[20:21], v[128:129]
	v_pk_mul_f32 v[146:147], v[22:23], v[130:131]
	global_store_dwordx4 v2, v[132:135], s[34:35]
	global_store_dwordx4 v2, v[136:139], s[34:35] offset:16
	global_store_dwordx4 v2, v[140:143], s[34:35] offset:2048
	global_store_dwordx4 v2, v[144:147], s[34:35] offset:2064
	s_waitcnt vmcnt(28)
	v_add_f32_dpp v112, v110, v110 quad_perm:[1,0,3,2] row_mask:0xf bank_mask:0xf
	s_mov_b64 s[36:37], s[24:25]
	s_add_u32 s24, s24, s22
	v_add_f32_dpp v112, v112, v112 quad_perm:[2,3,0,1] row_mask:0xf bank_mask:0xf
	s_addc_u32 s25, s25, 0
	s_nop 0
	v_add_f32_dpp v112, v112, v112 row_half_mirror row_mask:0xf bank_mask:0xf
	s_nop 1
	v_add_f32_dpp v112, v112, v112 row_mirror row_mask:0xf bank_mask:0xf
	v_fmamk_f32 v112, v112, 0x3a800000, v5
	v_rsq_f32_e32 v114, v112
	v_lshlrev_b32_e32 v116, 16, v102
	v_and_b32_e32 v117, 0xffff0000, v102
	v_lshlrev_b32_e32 v118, 16, v103
	v_and_b32_e32 v119, 0xffff0000, v103
	v_lshlrev_b32_e32 v120, 16, v104
	v_and_b32_e32 v121, 0xffff0000, v104
	v_lshlrev_b32_e32 v122, 16, v105
	v_and_b32_e32 v123, 0xffff0000, v105
	v_lshlrev_b32_e32 v124, 16, v106
	v_and_b32_e32 v125, 0xffff0000, v106
	v_lshlrev_b32_e32 v126, 16, v107
	v_and_b32_e32 v127, 0xffff0000, v107
	v_lshlrev_b32_e32 v128, 16, v108
	v_and_b32_e32 v129, 0xffff0000, v108
	v_lshlrev_b32_e32 v130, 16, v109
	v_and_b32_e32 v131, 0xffff0000, v109
	v_pk_mul_f32 v[116:117], v[114:115], v[116:117] op_sel_hi:[0,1]
	v_pk_mul_f32 v[118:119], v[114:115], v[118:119] op_sel_hi:[0,1]
	v_pk_mul_f32 v[120:121], v[114:115], v[120:121] op_sel_hi:[0,1]
	v_pk_mul_f32 v[122:123], v[114:115], v[122:123] op_sel_hi:[0,1]
	v_pk_mul_f32 v[124:125], v[114:115], v[124:125] op_sel_hi:[0,1]
	v_pk_mul_f32 v[126:127], v[114:115], v[126:127] op_sel_hi:[0,1]
	v_pk_mul_f32 v[128:129], v[114:115], v[128:129] op_sel_hi:[0,1]
	v_pk_mul_f32 v[130:131], v[114:115], v[130:131] op_sel_hi:[0,1]
	v_pk_mul_f32 v[132:133], v[8:9], v[116:117]
	v_pk_mul_f32 v[134:135], v[10:11], v[118:119]
	v_pk_mul_f32 v[136:137], v[12:13], v[120:121]
	v_pk_mul_f32 v[138:139], v[14:15], v[122:123]
	v_pk_mul_f32 v[140:141], v[16:17], v[124:125]
	v_pk_mul_f32 v[142:143], v[18:19], v[126:127]
	v_pk_mul_f32 v[144:145], v[20:21], v[128:129]
	v_pk_mul_f32 v[146:147], v[22:23], v[130:131]
	global_store_dwordx4 v2, v[132:135], s[36:37]
	global_store_dwordx4 v2, v[136:139], s[36:37] offset:16
	global_store_dwordx4 v2, v[140:143], s[36:37] offset:2048
	global_store_dwordx4 v2, v[144:147], s[36:37] offset:2064
.Lfin_tail:
	s_cmp_lt_i32 s12, 0x10000
	s_cbranch_scc0 .LBB0_3641
	s_mov_b64 s[26:27], s[16:17]
	s_mov_b64 s[28:29], s[18:19]
	global_load_dword v40, v4, s[26:27]
	global_load_dwordx4 v[32:35], v3, s[28:29]
	global_load_dwordx4 v[36:39], v3, s[28:29] offset:1024
	s_add_u32 s16, s16, s20
	s_addc_u32 s17, s17, 0
	s_add_u32 s18, s18, s21
	s_addc_u32 s19, s19, 0
	s_add_i32 s12, s12, s13
	s_waitcnt vmcnt(0)
	v_add_f32_dpp v112, v40, v40 quad_perm:[1,0,3,2] row_mask:0xf bank_mask:0xf
	s_mov_b64 s[34:35], s[24:25]
	s_add_u32 s24, s24, s22
	v_add_f32_dpp v112, v112, v112 quad_perm:[2,3,0,1] row_mask:0xf bank_mask:0xf
	s_addc_u32 s25, s25, 0
	s_nop 0
	v_add_f32_dpp v112, v112, v112 row_half_mirror row_mask:0xf bank_mask:0xf
	s_nop 1
	v_add_f32_dpp v112, v112, v112 row_mirror row_mask:0xf bank_mask:0xf
	v_fmamk_f32 v112, v112, 0x3a800000, v5
	v_rsq_f32_e32 v114, v112
	v_lshlrev_b32_e32 v116, 16, v32
	v_and_b32_e32 v117, 0xffff0000, v32
	v_lshlrev_b32_e32 v118, 16, v33
	v_and_b32_e32 v119, 0xffff0000, v33
	v_lshlrev_b32_e32 v120, 16, v34
	v_and_b32_e32 v121, 0xffff0000, v34
	v_lshlrev_b32_e32 v122, 16, v35
	v_and_b32_e32 v123, 0xffff0000, v35
	v_lshlrev_b32_e32 v124, 16, v36
	v_and_b32_e32 v125, 0xffff0000, v36
	v_lshlrev_b32_e32 v126, 16, v37
	v_and_b32_e32 v127, 0xffff0000, v37
	v_lshlrev_b32_e32 v128, 16, v38
	v_and_b32_e32 v129, 0xffff0000, v38
	v_lshlrev_b32_e32 v130, 16, v39
	v_and_b32_e32 v131, 0xffff0000, v39
	v_pk_mul_f32 v[116:117], v[114:115], v[116:117] op_sel_hi:[0,1]
	v_pk_mul_f32 v[118:119], v[114:115], v[118:119] op_sel_hi:[0,1]
	v_pk_mul_f32 v[120:121], v[114:115], v[120:121] op_sel_hi:[0,1]
	v_pk_mul_f32 v[122:123], v[114:115], v[122:123] op_sel_hi:[0,1]
	v_pk_mul_f32 v[124:125], v[114:115], v[124:125] op_sel_hi:[0,1]
	v_pk_mul_f32 v[126:127], v[114:115], v[126:127] op_sel_hi:[0,1]
	v_pk_mul_f32 v[128:129], v[114:115], v[128:129] op_sel_hi:[0,1]
	v_pk_mul_f32 v[130:131], v[114:115], v[130:131] op_sel_hi:[0,1]
	v_pk_mul_f32 v[132:133], v[8:9], v[116:117]
	v_pk_mul_f32 v[134:135], v[10:11], v[118:119]
	v_pk_mul_f32 v[136:137], v[12:13], v[120:121]
	v_pk_mul_f32 v[138:139], v[14:15], v[122:123]
	v_pk_mul_f32 v[140:141], v[16:17], v[124:125]
	v_pk_mul_f32 v[142:143], v[18:19], v[126:127]
	v_pk_mul_f32 v[144:145], v[20:21], v[128:129]
	v_pk_mul_f32 v[146:147], v[22:23], v[130:131]
	global_store_dwordx4 v2, v[132:135], s[34:35]
	global_store_dwordx4 v2, v[136:139], s[34:35] offset:16
	global_store_dwordx4 v2, v[140:143], s[34:35] offset:2048
	global_store_dwordx4 v2, v[144:147], s[34:35] offset:2064
	s_branch .Lfin_tail

	.amdhsa_kernel _Z8yoco_fwd4Args
		.amdhsa_group_segment_fixed_size 0
		.amdhsa_private_segment_fixed_size 0
		.amdhsa_kernarg_size 472
		.amdhsa_user_sgpr_count 2
		.amdhsa_user_sgpr_dispatch_ptr 0
		.amdhsa_user_sgpr_queue_ptr 0
		.amdhsa_user_sgpr_kernarg_segment_ptr 1
		.amdhsa_user_sgpr_dispatch_id 0
		.amdhsa_user_sgpr_kernarg_preload_length 0
		.amdhsa_user_sgpr_kernarg_preload_offset 0
		.amdhsa_user_sgpr_private_segment_size 0
		.amdhsa_uses_dynamic_stack 0
		.amdhsa_enable_private_segment 0
		.amdhsa_system_sgpr_workgroup_id_x 1
		.amdhsa_system_sgpr_workgroup_id_y 0
		.amdhsa_system_sgpr_workgroup_id_z 0
		.amdhsa_system_sgpr_workgroup_info 0
		.amdhsa_system_vgpr_workitem_id 0
		.amdhsa_next_free_vgpr 256
		.amdhsa_next_free_sgpr 98
		.amdhsa_accum_offset 256
		.amdhsa_reserve_vcc 1
		.amdhsa_float_round_mode_32 0
		.amdhsa_float_round_mode_16_64 0
		.amdhsa_float_denorm_mode_32 3
		.amdhsa_float_denorm_mode_16_64 3
		.amdhsa_dx10_clamp 1
		.amdhsa_ieee_mode 1
		.amdhsa_fp16_overflow 0
		.amdhsa_tg_split 0
		.amdhsa_exception_fp_ieee_invalid_op 0
		.amdhsa_exception_fp_denorm_src 0
		.amdhsa_exception_fp_ieee_div_zero 0
		.amdhsa_exception_fp_ieee_overflow 0
		.amdhsa_exception_fp_ieee_underflow 0
		.amdhsa_exception_fp_ieee_inexact 0
		.amdhsa_exception_int_div_zero 0
	.end_amdhsa_kernel

amdhsa.kernels:
  - .agpr_count:     0
    .args:
      - .offset:         0
        .size:           216
        .value_kind:     by_value
      - .offset:         216
        .size:           4
        .value_kind:     hidden_block_count_x
      - .offset:         220
        .size:           4
        .value_kind:     hidden_block_count_y
      - .offset:         224
        .size:           4
        .value_kind:     hidden_block_count_z
      - .offset:         228
        .size:           2
        .value_kind:     hidden_group_size_x
      - .offset:         230
        .size:           2
        .value_kind:     hidden_group_size_y
      - .offset:         232
        .size:           2
        .value_kind:     hidden_group_size_z
      - .offset:         234
        .size:           2
        .value_kind:     hidden_remainder_x
      - .offset:         236
        .size:           2
        .value_kind:     hidden_remainder_y
      - .offset:         238
        .size:           2
        .value_kind:     hidden_remainder_z
      - .offset:         256
        .size:           8
        .value_kind:     hidden_global_offset_x
      - .offset:         264
        .size:           8
        .value_kind:     hidden_global_offset_y
      - .offset:         272
        .size:           8
        .value_kind:     hidden_global_offset_z
      - .offset:         280
        .size:           2
        .value_kind:     hidden_grid_dims
      - .offset:         336
        .size:           4
        .value_kind:     hidden_dynamic_lds_size
    .group_segment_fixed_size: 0
    .kernarg_segment_align: 8
    .kernarg_segment_size: 472
    .language:       OpenCL C
    .language_version:
      - 2
      - 0
    .max_flat_workgroup_size: 512
    .name:           _Z8yoco_fwd4Args
    .private_segment_fixed_size: 0
    .sgpr_count:     104
    .sgpr_spill_count: 33
    .symbol:         _Z8yoco_fwd4Args.kd
    .uniform_work_group_size: 1
    .uses_dynamic_stack: false
    .vgpr_count:     256
    .vgpr_spill_count: 0
    .wavefront_size: 64
